# v27: v24 + quarter-rate v_mul_lo_u32 (pixel*72) replaced by full-rate v_mul_u32_u24 in both k_nca tile/Q load address chains (bit-exact, operands < 2^14)
# speedup vs baseline: 1.0183x; 1.0183x over previous
_Z5k_ncaILi0EEvPKDF16_S1_PKfS3_PDF16_S3_S3_S3_S3_Pf:
	s_load_dwordx4 s[12:15], s[0:1], 0x0
	s_lshl_b32 s3, s2, 1
	s_and_b32 s3, s3, 12
	s_lshr_b32 s4, s2, 6
	v_lshrrev_b32_e32 v1, 5, v0
	s_add_i32 s3, s3, s4
	s_lshl_b32 s4, s2, 6
	v_and_b32_e32 v62, 4, v1
	v_lshrrev_b32_e32 v1, 4, v0
	s_and_b32 s4, s4, 64
	s_and_b32 s2, s2, 56
	v_and_b32_e32 v63, 4, v1
	v_bfe_u32 v1, v0, 2, 2
	s_lshl_b32 s20, s3, 3
	s_or_b32 s21, s4, s2
	v_or3_b32 v2, v62, s20, v1
	v_and_b32_e32 v61, 3, v0
	v_lshl_or_b32 v2, v2, 7, s21
	v_or3_b32 v2, v2, v63, v61
	s_movk_i32 s4, 0x48
	v_mul_u32_u24_e32 v54, s4, v2
	v_mov_b32_e32 v55, 0
	s_waitcnt lgkmcnt(0)
	v_lshl_add_u64 v[6:7], v[54:55], 1, s[12:13]
	v_and_b32_e32 v2, 48, v0
	v_mov_b32_e32 v3, v55
	v_lshl_add_u64 v[8:9], v[6:7], 0, v[2:3]
	global_load_dwordx4 v[2:5], v[8:9], off offset:64
	global_load_dwordx4 v[10:13], v[8:9], off
	global_load_dwordx4 v[22:25], v[6:7], off offset:128
	v_mul_u32_u24_e32 v6, 0x1c72, v0
	v_mul_u32_u24_e32 v65, 0x195, v0
	s_movk_i32 s2, 0xffee
	s_add_i32 s20, s20, -5
	s_add_i32 s21, s21, -5
	v_lshrrev_b32_e32 v64, 16, v6
	v_mul_i32_i24_sdwa v6, v65, s2 dst_sel:DWORD dst_unused:UNUSED_PAD src0_sel:WORD_1 src1_sel:DWORD
	v_add_u32_sdwa v14, s20, v65 dst_sel:DWORD dst_unused:UNUSED_PAD src0_sel:DWORD src1_sel:WORD_1
	v_add3_u32 v15, s21, v64, v6
	v_or_b32_e32 v6, v15, v14
	s_movk_i32 s5, 0x80
	v_cmp_gt_u32_e32 vcc, s5, v6
	v_mov_b64_e32 v[6:7], 0
	v_mov_b64_e32 v[8:9], 0
	s_and_saveexec_b64 s[2:3], vcc
	v_lshl_or_b32 v9, v14, 7, v15
	v_mad_i32_i24 v8, v64, -9, v0
	v_mul_u32_u24_e32 v9, s4, v9
	v_lshl_add_u32 v8, v8, 3, v9
	v_ashrrev_i32_e32 v9, 31, v8
	s_or_b64 exec, exec, s[2:3]
	v_lshl_add_u64 v[8:9], v[8:9], 1, s[14:15]
	global_load_dwordx4 v[26:29], v[8:9], off
	v_or_b32_e32 v59, 0x200, v0
	v_mul_u32_u24_e32 v8, 0x1c72, v59
	v_lshrrev_b32_e32 v66, 16, v8
	v_mul_u32_u24_e32 v8, 0x653, v59
	v_lshrrev_b32_e32 v67, 18, v8
	v_mul_i32_i24_e32 v9, 0xffffffee, v67
	v_add_u32_e32 v8, s20, v67
	v_add3_u32 v9, s21, v66, v9
	v_or_b32_e32 v14, v9, v8
	v_cmp_gt_u32_e64 s[2:3], s5, v14
	s_and_saveexec_b64 s[4:5], s[2:3]
	v_lshl_or_b32 v7, v8, 7, v9
	s_movk_i32 s6, 0x48
	v_mad_i32_i24 v6, v66, -9, v59
	v_mul_u32_u24_e32 v7, s6, v7
	v_lshl_add_u32 v6, v6, 3, v7
	v_ashrrev_i32_e32 v7, 31, v6
	s_or_b64 exec, exec, s[4:5]
	v_lshl_add_u64 v[6:7], v[6:7], 1, s[14:15]
	global_load_dwordx4 v[30:33], v[6:7], off
	v_or_b32_e32 v58, 0x400, v0
	v_mul_u32_u24_e32 v6, 0x1c72, v58
	v_lshrrev_b32_e32 v68, 16, v6
	v_mul_u32_u24_e32 v6, 0x653, v58
	v_lshrrev_b32_e32 v69, 18, v6
	v_mul_i32_i24_e32 v6, 0xffffffee, v69
	v_add_u32_e32 v14, s20, v69
	v_add3_u32 v15, s21, v68, v6
	v_or_b32_e32 v6, v15, v14
	s_movk_i32 s8, 0x80
	v_cmp_gt_u32_e64 s[4:5], s8, v6
	v_mov_b64_e32 v[6:7], 0
	v_mov_b64_e32 v[8:9], 0
	s_and_saveexec_b64 s[6:7], s[4:5]
	v_lshl_or_b32 v9, v14, 7, v15
	s_movk_i32 s9, 0x48
	v_mad_i32_i24 v8, v68, -9, v58
	v_mul_u32_u24_e32 v9, s9, v9
	v_lshl_add_u32 v8, v8, 3, v9
	v_mov_b32_e32 v9, 0
	s_or_b64 exec, exec, s[6:7]
	v_lshl_add_u64 v[8:9], v[8:9], 1, s[14:15]
	global_load_dwordx4 v[34:37], v[8:9], off
	v_or_b32_e32 v70, 0x600, v0
	v_mul_u32_u24_e32 v8, 0x1c72, v70
	v_lshrrev_b32_e32 v71, 16, v8
	v_mul_u32_u24_e32 v8, 0x653, v70
	v_lshrrev_b32_e32 v72, 18, v8
	v_mul_i32_i24_e32 v9, 0xffffffee, v72
	v_add_u32_e32 v8, s20, v72
	v_add3_u32 v9, s21, v71, v9
	v_or_b32_e32 v14, v9, v8
	v_cmp_gt_u32_e64 s[8:9], s8, v14
	s_and_saveexec_b64 s[6:7], s[8:9]
	v_lshl_or_b32 v7, v8, 7, v9
	s_movk_i32 s10, 0x48
	v_mad_i32_i24 v6, v71, -9, v70
	v_mul_u32_u24_e32 v7, s10, v7
	v_lshl_add_u32 v6, v6, 3, v7
	v_mov_b32_e32 v7, 0
	s_or_b64 exec, exec, s[6:7]
	v_lshl_add_u64 v[6:7], v[6:7], 1, s[14:15]
	global_load_dwordx4 v[42:45], v[6:7], off
	v_or_b32_e32 v73, 0x800, v0
	v_mul_u32_u24_e32 v6, 0x1c72, v73
	v_lshrrev_b32_e32 v14, 16, v6
	v_mul_u32_u24_e32 v6, 0xca5, v73
	s_load_dwordx2 s[12:13], s[0:1], 0x18
	v_lshrrev_b32_e32 v6, 19, v6
	v_mul_i32_i24_e32 v7, 0xffffffee, v6
	v_add_u32_e32 v15, s20, v6
	v_add3_u32 v16, s21, v14, v7
	v_or_b32_e32 v6, v16, v15
	s_movk_i32 s18, 0x80
	v_cmp_gt_u32_e64 s[10:11], s18, v6
	v_mov_b64_e32 v[6:7], 0
	v_mov_b64_e32 v[8:9], 0
	s_and_saveexec_b64 s[6:7], s[10:11]
	v_lshl_or_b32 v9, v15, 7, v16
	s_movk_i32 s16, 0x48
	v_mad_i32_i24 v8, v14, -9, v73
	v_mul_u32_u24_e32 v9, s16, v9
	v_lshl_add_u32 v8, v8, 3, v9
	v_mov_b32_e32 v9, 0
	s_or_b64 exec, exec, s[6:7]
	v_lshl_add_u64 v[8:9], v[8:9], 1, s[14:15]
	global_load_dwordx4 v[46:49], v[8:9], off
	v_or_b32_e32 v74, 0xa00, v0
	v_min_u32_e32 v8, 0xb63, v74
	v_mul_u32_u24_e32 v14, 0xca5, v8
	s_load_dwordx2 s[16:17], s[0:1], 0x10
	s_load_dwordx2 s[64:65], s[0:1], 0x20
	v_mul_u32_u24_e32 v9, 0x1c72, v8
	v_lshrrev_b32_e32 v14, 19, v14
	v_lshrrev_b32_e32 v9, 16, v9
	v_mul_i32_i24_e32 v15, 0xffffffee, v14
	v_add_u32_e32 v14, s20, v14
	v_add3_u32 v15, s21, v9, v15
	v_or_b32_e32 v16, v15, v14
	v_cmp_gt_u32_e64 s[6:7], s18, v16
	s_and_saveexec_b64 s[18:19], s[6:7]
	v_lshl_or_b32 v7, v14, 7, v15
	s_movk_i32 s22, 0x48
	v_mad_i32_i24 v6, v9, -9, v8
	v_mul_u32_u24_e32 v7, s22, v7
	v_lshl_add_u32 v6, v6, 3, v7
	v_mov_b32_e32 v7, 0
	s_or_b64 exec, exec, s[18:19]
	v_lshl_add_u64 v[6:7], v[6:7], 1, s[14:15]
	s_movk_i32 s14, 0xe39
	global_load_dwordx4 v[38:41], v[6:7], off
	v_mul_u32_u24_sdwa v6, v0, s14 dst_sel:DWORD dst_unused:UNUSED_PAD src0_sel:WORD_0 src1_sel:DWORD
	v_lshrrev_b32_e32 v60, 16, v6
	v_or_b32_e32 v14, 0x200, v0
	s_movk_i32 s14, 0xffee
	s_movk_i32 s15, 0x48
	v_mul_u32_u24_e32 v6, 0x48, v60
	v_mul_u32_u24_e32 v8, 0xe39, v14
	v_mad_i32_i24 v52, v60, s14, v0
	v_lshlrev_b32_e32 v50, 2, v6
	v_mov_b32_e32 v51, 0
	v_mul_i32_i24_sdwa v15, v8, s14 dst_sel:DWORD dst_unused:UNUSED_PAD src0_sel:WORD_1 src1_sel:DWORD
	v_mul_u32_u24_sdwa v8, v8, s15 dst_sel:DWORD dst_unused:UNUSED_PAD src0_sel:WORD_1 src1_sel:DWORD
	s_waitcnt lgkmcnt(0)
	v_lshl_add_u64 v[6:7], s[16:17], 0, v[50:51]
	v_lshlrev_b32_e32 v56, 2, v52
	v_lshlrev_b32_e32 v50, 2, v8
	v_add_lshl_u32 v14, v15, v14, 2
	v_ashrrev_i32_e32 v57, 31, v56
	v_lshl_add_u64 v[8:9], s[16:17], 0, v[50:51]
	v_ashrrev_i32_e32 v15, 31, v14
	v_lshl_add_u64 v[6:7], v[56:57], 2, v[6:7]
	v_lshl_add_u64 v[8:9], v[14:15], 2, v[8:9]
	global_load_dwordx4 v[18:21], v[6:7], off
	global_load_dwordx4 v[14:17], v[8:9], off
	v_min_u32_e32 v8, 0x50f, v58
	v_mul_u32_u24_e32 v6, 0xe39, v8
	v_mul_i32_i24_sdwa v9, v6, s14 dst_sel:DWORD dst_unused:UNUSED_PAD src0_sel:WORD_1 src1_sel:DWORD
	v_mul_u32_u24_sdwa v6, v6, s15 dst_sel:DWORD dst_unused:UNUSED_PAD src0_sel:WORD_1 src1_sel:DWORD
	v_lshlrev_b32_e32 v50, 2, v6
	v_add_lshl_u32 v8, v9, v8, 2
	v_lshl_add_u64 v[6:7], s[16:17], 0, v[50:51]
	v_ashrrev_i32_e32 v9, 31, v8
	v_min_u32_e32 v50, 0x47, v0
	v_lshl_add_u64 v[6:7], v[8:9], 2, v[6:7]
	v_lshlrev_b32_e32 v50, 2, v50
	global_load_dwordx4 v[6:9], v[6:7], off
	s_nop 0
	global_load_dword v57, v50, s[12:13]
	s_movk_i32 s12, 0x144
	v_cmp_gt_u32_e64 s[12:13], s12, v0
	s_and_saveexec_b64 s[14:15], s[12:13]
	s_cbranch_execz .LBB1_14
	v_mul_i32_i24_e32 v50, 0x1c72, v52
	v_lshrrev_b32_e32 v53, 31, v50
	v_add_u16_sdwa v50, v50, v53 dst_sel:DWORD dst_unused:UNUSED_PAD src0_sel:WORD_1 src1_sel:DWORD
	v_bfe_i32 v50, v50, 0, 16
	v_mul_i32_i24_e32 v53, -9, v50
	v_mad_u32_u24 v50, v60, 20, v50
	v_mul_i32_i24_e32 v50, 0xa0, v50
	v_add_lshl_u32 v52, v53, v52, 4
	v_add3_u32 v75, v50, 0, v52
	v_mov_b32_e32 v50, v51
	v_mov_b32_e32 v52, v51
	v_mov_b32_e32 v53, v51
	ds_write_b128 v75, v[50:53] offset:2880

_Z5k_ncaILi1EEvPKDF16_S1_PKfS3_PDF16_S3_S3_S3_S3_Pf:
	s_load_dwordx4 s[20:23], s[0:1], 0x0
	s_lshl_b32 s3, s2, 1
	s_and_b32 s3, s3, 12
	s_lshr_b32 s4, s2, 6
	s_add_i32 s3, s3, s4
	v_lshrrev_b32_e32 v1, 5, v0
	s_lshl_b32 s4, s2, 6
	v_and_b32_e32 v76, 4, v1
	s_lshl_b32 s29, s3, 3
	s_and_b32 s4, s4, 64
	s_and_b32 s2, s2, 56
	v_bfe_u32 v60, v0, 2, 2
	v_or_b32_e32 v58, s29, v76
	s_or_b32 s28, s4, s2
	v_lshrrev_b32_e32 v52, 4, v0
	v_or_b32_e32 v2, v58, v60
	v_and_b32_e32 v57, 4, v52
	v_and_b32_e32 v1, 3, v0
	v_lshl_or_b32 v2, v2, 7, s28
	v_or3_b32 v56, v2, v57, v1
	s_movk_i32 s4, 0x48
	v_mul_u32_u24_e32 v2, s4, v56
	v_mov_b32_e32 v3, 0
	s_waitcnt lgkmcnt(0)
	v_lshl_add_u64 v[6:7], v[2:3], 1, s[20:21]
	v_and_b32_e32 v2, 48, v0
	v_lshl_add_u64 v[8:9], v[6:7], 0, v[2:3]
	global_load_dwordx4 v[2:5], v[8:9], off offset:64
	global_load_dwordx4 v[10:13], v[8:9], off
	global_load_dwordx4 v[22:25], v[6:7], off offset:128
	v_mul_u32_u24_e32 v6, 0x1c72, v0
	v_mul_u32_u24_e32 v78, 0x195, v0
	s_movk_i32 s2, 0xffee
	s_add_i32 s29, s29, -5
	s_add_i32 s30, s28, -5
	v_lshrrev_b32_e32 v77, 16, v6
	v_mul_i32_i24_sdwa v6, v78, s2 dst_sel:DWORD dst_unused:UNUSED_PAD src0_sel:WORD_1 src1_sel:DWORD
	v_add_u32_sdwa v14, s29, v78 dst_sel:DWORD dst_unused:UNUSED_PAD src0_sel:DWORD src1_sel:WORD_1
	v_add3_u32 v15, s30, v77, v6
	v_or_b32_e32 v6, v15, v14
	s_movk_i32 s5, 0x80
	v_cmp_gt_u32_e32 vcc, s5, v6
	v_mov_b64_e32 v[6:7], 0
	v_mov_b64_e32 v[8:9], 0
	s_and_saveexec_b64 s[2:3], vcc
	v_lshl_or_b32 v9, v14, 7, v15
	v_mad_i32_i24 v8, v77, -9, v0
	v_mul_u32_u24_e32 v9, s4, v9
	v_lshl_add_u32 v8, v8, 3, v9
	v_ashrrev_i32_e32 v9, 31, v8
	s_or_b64 exec, exec, s[2:3]
	v_lshl_add_u64 v[8:9], v[8:9], 1, s[22:23]
	global_load_dwordx4 v[26:29], v[8:9], off
	v_or_b32_e32 v62, 0x200, v0
	v_mul_u32_u24_e32 v8, 0x1c72, v62
	v_lshrrev_b32_e32 v79, 16, v8
	v_mul_u32_u24_e32 v8, 0x653, v62
	v_lshrrev_b32_e32 v80, 18, v8
	v_mul_i32_i24_e32 v9, 0xffffffee, v80
	v_add_u32_e32 v8, s29, v80
	v_add3_u32 v9, s30, v79, v9
	v_or_b32_e32 v14, v9, v8
	v_cmp_gt_u32_e64 s[2:3], s5, v14
	s_and_saveexec_b64 s[4:5], s[2:3]
	v_lshl_or_b32 v7, v8, 7, v9
	s_movk_i32 s6, 0x48
	v_mad_i32_i24 v6, v79, -9, v62
	v_mul_u32_u24_e32 v7, s6, v7
	v_lshl_add_u32 v6, v6, 3, v7
	v_ashrrev_i32_e32 v7, 31, v6
	s_or_b64 exec, exec, s[4:5]
	v_lshl_add_u64 v[6:7], v[6:7], 1, s[22:23]
	global_load_dwordx4 v[30:33], v[6:7], off
	v_or_b32_e32 v61, 0x400, v0
	v_mul_u32_u24_e32 v6, 0x1c72, v61
	v_lshrrev_b32_e32 v81, 16, v6
	v_mul_u32_u24_e32 v6, 0x653, v61
	v_lshrrev_b32_e32 v82, 18, v6
	v_mul_i32_i24_e32 v6, 0xffffffee, v82
	v_add_u32_e32 v14, s29, v82
	v_add3_u32 v15, s30, v81, v6
	v_or_b32_e32 v6, v15, v14
	s_movk_i32 s8, 0x80
	v_cmp_gt_u32_e64 s[4:5], s8, v6
	v_mov_b64_e32 v[6:7], 0
	v_mov_b64_e32 v[8:9], 0
	s_and_saveexec_b64 s[6:7], s[4:5]
	v_lshl_or_b32 v9, v14, 7, v15
	s_movk_i32 s9, 0x48
	v_mad_i32_i24 v8, v81, -9, v61
	v_mul_u32_u24_e32 v9, s9, v9
	v_lshl_add_u32 v8, v8, 3, v9
	v_mov_b32_e32 v9, 0
	s_or_b64 exec, exec, s[6:7]
	v_lshl_add_u64 v[8:9], v[8:9], 1, s[22:23]
	global_load_dwordx4 v[34:37], v[8:9], off
	v_or_b32_e32 v83, 0x600, v0
	v_mul_u32_u24_e32 v8, 0x1c72, v83
	v_lshrrev_b32_e32 v84, 16, v8
	v_mul_u32_u24_e32 v8, 0x653, v83
	v_lshrrev_b32_e32 v85, 18, v8
	v_mul_i32_i24_e32 v9, 0xffffffee, v85
	v_add_u32_e32 v8, s29, v85
	v_add3_u32 v9, s30, v84, v9
	v_or_b32_e32 v14, v9, v8
	v_cmp_gt_u32_e64 s[8:9], s8, v14
	s_and_saveexec_b64 s[6:7], s[8:9]
	v_lshl_or_b32 v7, v8, 7, v9
	s_movk_i32 s10, 0x48
	v_mad_i32_i24 v6, v84, -9, v83
	v_mul_u32_u24_e32 v7, s10, v7
	v_lshl_add_u32 v6, v6, 3, v7
	v_mov_b32_e32 v7, 0
	s_or_b64 exec, exec, s[6:7]
	v_lshl_add_u64 v[6:7], v[6:7], 1, s[22:23]
	global_load_dwordx4 v[42:45], v[6:7], off
	v_or_b32_e32 v86, 0x800, v0
	v_mul_u32_u24_e32 v6, 0x1c72, v86
	v_lshrrev_b32_e32 v14, 16, v6
	v_mul_u32_u24_e32 v6, 0xca5, v86
	s_load_dwordx8 s[12:19], s[0:1], 0x28
	s_load_dwordx2 s[20:21], s[0:1], 0x18
	v_lshrrev_b32_e32 v6, 19, v6
	v_mul_i32_i24_e32 v7, 0xffffffee, v6
	v_add_u32_e32 v15, s29, v6
	v_add3_u32 v16, s30, v14, v7
	v_or_b32_e32 v6, v16, v15
	s_movk_i32 s26, 0x80
	v_cmp_gt_u32_e64 s[10:11], s26, v6
	v_mov_b64_e32 v[6:7], 0
	v_mov_b64_e32 v[8:9], 0
	s_and_saveexec_b64 s[6:7], s[10:11]
	v_lshl_or_b32 v9, v15, 7, v16
	s_movk_i32 s24, 0x48
	v_mad_i32_i24 v8, v14, -9, v86
	v_mul_u32_u24_e32 v9, s24, v9
	v_lshl_add_u32 v8, v8, 3, v9
	v_mov_b32_e32 v9, 0
	s_or_b64 exec, exec, s[6:7]
	v_lshl_add_u64 v[8:9], v[8:9], 1, s[22:23]
	global_load_dwordx4 v[46:49], v[8:9], off
	v_or_b32_e32 v87, 0xa00, v0
	v_min_u32_e32 v8, 0xb63, v87
	v_mul_u32_u24_e32 v14, 0xca5, v8
	s_load_dwordx2 s[24:25], s[0:1], 0x10
	s_load_dwordx2 s[64:65], s[0:1], 0x48
	v_mul_u32_u24_e32 v9, 0x1c72, v8
	v_lshrrev_b32_e32 v14, 19, v14
	v_lshrrev_b32_e32 v9, 16, v9
	v_mul_i32_i24_e32 v15, 0xffffffee, v14
	v_add_u32_e32 v14, s29, v14
	v_add3_u32 v15, s30, v9, v15
	v_or_b32_e32 v16, v15, v14
	v_and_b32_e32 v59, 15, v0
	v_cmp_gt_u32_e64 s[6:7], s26, v16
	s_and_saveexec_b64 s[26:27], s[6:7]
	v_lshl_or_b32 v7, v14, 7, v15
	s_movk_i32 s31, 0x48
	v_mad_i32_i24 v6, v9, -9, v8
	v_mul_u32_u24_e32 v7, s31, v7
	v_lshl_add_u32 v6, v6, 3, v7
	v_mov_b32_e32 v7, 0
	s_or_b64 exec, exec, s[26:27]
	v_lshl_add_u64 v[6:7], v[6:7], 1, s[22:23]
	s_movk_i32 s22, 0xe39
	global_load_dwordx4 v[38:41], v[6:7], off
	v_mul_u32_u24_sdwa v6, v0, s22 dst_sel:DWORD dst_unused:UNUSED_PAD src0_sel:WORD_0 src1_sel:DWORD
	v_lshrrev_b32_e32 v75, 16, v6
	v_or_b32_e32 v14, 0x200, v0
	s_movk_i32 s22, 0xffee
	s_movk_i32 s23, 0x48
	v_mul_u32_u24_e32 v6, 0x48, v75
	v_mul_u32_u24_e32 v8, 0xe39, v14
	v_mad_i32_i24 v53, v75, s22, v0
	v_lshlrev_b32_e32 v50, 2, v6
	v_mov_b32_e32 v51, 0
	v_mul_i32_i24_sdwa v15, v8, s22 dst_sel:DWORD dst_unused:UNUSED_PAD src0_sel:WORD_1 src1_sel:DWORD
	v_mul_u32_u24_sdwa v8, v8, s23 dst_sel:DWORD dst_unused:UNUSED_PAD src0_sel:WORD_1 src1_sel:DWORD
	s_waitcnt lgkmcnt(0)
	v_lshl_add_u64 v[6:7], s[24:25], 0, v[50:51]
	v_lshlrev_b32_e32 v54, 2, v53
	v_lshlrev_b32_e32 v50, 2, v8
	v_add_lshl_u32 v14, v15, v14, 2
	v_ashrrev_i32_e32 v55, 31, v54
	v_lshl_add_u64 v[8:9], s[24:25], 0, v[50:51]
	v_ashrrev_i32_e32 v15, 31, v14
	v_lshl_add_u64 v[6:7], v[54:55], 2, v[6:7]
	v_lshl_add_u64 v[8:9], v[14:15], 2, v[8:9]
	global_load_dwordx4 v[18:21], v[6:7], off
	global_load_dwordx4 v[14:17], v[8:9], off
	v_min_u32_e32 v8, 0x50f, v61
	v_mul_u32_u24_e32 v6, 0xe39, v8
	v_mul_i32_i24_sdwa v9, v6, s22 dst_sel:DWORD dst_unused:UNUSED_PAD src0_sel:WORD_1 src1_sel:DWORD
	v_mul_u32_u24_sdwa v6, v6, s23 dst_sel:DWORD dst_unused:UNUSED_PAD src0_sel:WORD_1 src1_sel:DWORD
	v_lshlrev_b32_e32 v50, 2, v6
	v_lshl_add_u64 v[6:7], s[24:25], 0, v[50:51]
	v_min_u32_e32 v50, 0x47, v0
	v_add_lshl_u32 v8, v9, v8, 2
	v_lshlrev_b32_e32 v50, 2, v50
	v_add_u32_e32 v63, -8, v59
	v_ashrrev_i32_e32 v9, 31, v8
	global_load_dword v68, v50, s[20:21]
	v_min_u32_e32 v50, 6, v59
	v_med3_i32 v64, v63, 0, 2
	v_mul_u32_u24_e32 v52, 7, v52
	v_and_b32_e32 v72, 15, v62
	v_lshl_add_u64 v[6:7], v[8:9], 2, v[6:7]
	v_lshlrev_b32_e32 v55, 2, v50
	v_lshlrev_b32_e32 v65, 2, v64
	v_add_lshl_u32 v50, v52, v50, 2
	v_lshrrev_b32_e32 v52, 4, v62
	v_add_u32_e32 v71, -8, v72
	global_load_dwordx4 v[6:9], v[6:7], off
	v_med3_i32 v67, v71, 0, 2
	global_load_dword v55, v55, s[14:15]
	s_nop 0
	global_load_dword v64, v65, s[18:19]
	global_load_dword v70, v65, s[16:17]
	v_min_u32_e32 v65, 6, v72
	v_mul_u32_u24_e32 v52, 7, v52
	v_add_lshl_u32 v52, v52, v65, 2
	global_load_dword v66, v50, s[12:13]
	global_load_dword v65, v52, s[12:13]
	v_mad_u32_u24 v50, 64, 3, v67
	v_add_u32_e32 v50, 0xffffff40, v50
	v_lshl_add_u64 v[88:89], v[50:51], 2, s[16:17]
	v_min_u32_e32 v50, 0x47f, v61
	v_lshrrev_b32_e32 v52, 4, v50
	v_and_b32_e32 v50, 15, v50
	v_add_u32_e32 v69, -8, v50
	s_movk_i32 s14, 0xff40
	v_min_u32_e32 v67, 6, v50
	v_med3_i32 v50, v69, 0, 2
	v_mul_u32_u24_e32 v52, 3, v52
	v_add3_u32 v50, v52, v50, s14
	global_load_dword v74, v[88:89], off
	v_lshlrev_b32_e32 v67, 2, v67
	v_lshl_add_u64 v[88:89], v[50:51], 2, s[16:17]
	global_load_dword v67, v67, s[12:13] offset:1764
	s_movk_i32 s12, 0x144
	global_load_dword v73, v[88:89], off
	v_cmp_gt_u32_e64 s[12:13], s12, v0
	s_and_saveexec_b64 s[14:15], s[12:13]
	s_cbranch_execz .LBB2_14
	v_mul_i32_i24_e32 v50, 0x1c72, v53
	v_lshrrev_b32_e32 v52, 31, v50
	v_add_u16_sdwa v50, v50, v52 dst_sel:DWORD dst_unused:UNUSED_PAD src0_sel:WORD_1 src1_sel:DWORD
	v_bfe_i32 v50, v50, 0, 16
	v_mul_i32_i24_e32 v52, -9, v50
	v_mad_u32_u24 v50, v75, 20, v50
	v_mul_i32_i24_e32 v50, 0xa0, v50
	v_add_lshl_u32 v52, v52, v53, 4
	v_add3_u32 v88, v50, 0, v52
	v_mov_b32_e32 v50, v51
	v_mov_b32_e32 v52, v51
	v_mov_b32_e32 v53, v51
	ds_write_b128 v88, v[50:53] offset:2880
